# out-proj epilogue: single vmcnt(0) after the 16 residual loads replaced by a counted vmcnt(15) in front of each chunk so stores start while later loads are in flight
# speedup vs baseline: 1.0017x; 1.0017x over previous
.LBB0_508:
	s_add_u32 s4, s50, 0xfffc0080
	s_addc_u32 s52, s51, -1
	s_add_i32 s69, 0, 0x10000
	s_cmp_eq_u32 s68, 12
	s_cselect_b32 s55, s47, s52
	s_cselect_b32 s54, s64, s4
	s_cselect_b32 s53, s45, s67
	s_cselect_b32 s52, s65, s66
	s_add_i32 s4, 0, 0x14000
	v_add_u32_e32 v142, s69, v195
	v_add_u32_e32 v158, s4, v195
	ds_read_b128 v[130:133], v142
	ds_read_b128 v[134:137], v142 offset:1024
	ds_read_b128 v[138:141], v142 offset:2048
	ds_read_b128 v[142:145], v142 offset:3072
	ds_read_b128 v[146:149], v158
	ds_read_b128 v[150:153], v158 offset:1024
	ds_read_b128 v[154:157], v158 offset:2048
	ds_read_b128 v[158:161], v158 offset:3072
	v_lshl_add_u64 v[210:211], s[50:51], 0, v[202:203]
	s_add_i32 m0, s49, 0xc000
	ds_read_b128 v[162:165], v234
	ds_read_b128 v[166:169], v234 offset:1024
	ds_read_b128 v[170:173], v234 offset:2048
	ds_read_b128 v[174:177], v234 offset:3072
	ds_read_b128 v[178:181], v234 offset:4096
	ds_read_b128 v[182:185], v234 offset:5120
	ds_read_b128 v[186:189], v234 offset:6144
	ds_read_b128 v[206:209], v234 offset:7168
	global_load_lds_dwordx4 v[210:211], off
	v_lshl_add_u64 v[210:211], s[50:51], 0, v[204:205]
	s_add_i32 m0, s49, 0xe000
	s_nop 0
	global_load_lds_dwordx4 v[210:211], off
	s_waitcnt vmcnt(8)
	s_waitcnt lgkmcnt(0)
	s_barrier
	s_setprio 1
	s_waitcnt lgkmcnt(0)
	v_mfma_f32_16x16x32_bf16 v[126:129], v[130:133], v[162:165], v[126:129]
	v_mfma_f32_16x16x32_bf16 v[122:125], v[138:141], v[162:165], v[122:125]
	v_mfma_f32_16x16x32_bf16 v[110:113], v[130:133], v[170:173], v[110:113]
	v_mfma_f32_16x16x32_bf16 v[106:109], v[138:141], v[170:173], v[106:109]
	v_mfma_f32_16x16x32_bf16 v[98:101], v[130:133], v[178:181], v[98:101]
	v_mfma_f32_16x16x32_bf16 v[90:93], v[138:141], v[178:181], v[90:93]
	v_mfma_f32_16x16x32_bf16 v[82:85], v[130:133], v[186:189], v[82:85]
	v_mfma_f32_16x16x32_bf16 v[74:77], v[138:141], v[186:189], v[74:77]
	v_mfma_f32_16x16x32_bf16 v[126:129], v[134:137], v[166:169], v[126:129]
	v_mfma_f32_16x16x32_bf16 v[122:125], v[142:145], v[166:169], v[122:125]
	v_mfma_f32_16x16x32_bf16 v[110:113], v[134:137], v[174:177], v[110:113]
	v_mfma_f32_16x16x32_bf16 v[106:109], v[142:145], v[174:177], v[106:109]
	v_mfma_f32_16x16x32_bf16 v[98:101], v[134:137], v[182:185], v[98:101]
	v_mfma_f32_16x16x32_bf16 v[90:93], v[142:145], v[182:185], v[90:93]
	v_mfma_f32_16x16x32_bf16 v[82:85], v[134:137], v[206:209], v[82:85]
	v_mfma_f32_16x16x32_bf16 v[74:77], v[142:145], v[206:209], v[74:77]
	s_setprio 0
	s_setprio 1
	v_mfma_f32_16x16x32_bf16 v[118:121], v[146:149], v[162:165], v[118:121]
	v_mfma_f32_16x16x32_bf16 v[114:117], v[154:157], v[162:165], v[114:117]
	v_mfma_f32_16x16x32_bf16 v[102:105], v[146:149], v[170:173], v[102:105]
	v_mfma_f32_16x16x32_bf16 v[94:97], v[154:157], v[170:173], v[94:97]
	v_mfma_f32_16x16x32_bf16 v[86:89], v[146:149], v[178:181], v[86:89]
	v_mfma_f32_16x16x32_bf16 v[78:81], v[154:157], v[178:181], v[78:81]
	v_mfma_f32_16x16x32_bf16 v[70:73], v[146:149], v[186:189], v[70:73]
	v_mfma_f32_16x16x32_bf16 v[66:69], v[154:157], v[186:189], v[66:69]
	v_mfma_f32_16x16x32_bf16 v[118:121], v[150:153], v[166:169], v[118:121]
	v_mfma_f32_16x16x32_bf16 v[114:117], v[158:161], v[166:169], v[114:117]
	v_mfma_f32_16x16x32_bf16 v[102:105], v[150:153], v[174:177], v[102:105]
	v_mfma_f32_16x16x32_bf16 v[94:97], v[158:161], v[174:177], v[94:97]
	v_mfma_f32_16x16x32_bf16 v[86:89], v[150:153], v[182:185], v[86:89]
	v_mfma_f32_16x16x32_bf16 v[78:81], v[158:161], v[182:185], v[78:81]
	v_mfma_f32_16x16x32_bf16 v[70:73], v[150:153], v[206:209], v[70:73]
	v_mfma_f32_16x16x32_bf16 v[66:69], v[158:161], v[206:209], v[66:69]
	s_setprio 0
	s_barrier
	s_add_i32 s69, s69, s59
	v_lshl_add_u64 v[210:211], s[52:53], 0, v[0:1]
	s_mov_b32 m0, s69
	ds_read_b128 v[162:165], v234 offset:16384
	ds_read_b128 v[166:169], v234 offset:17408
	ds_read_b128 v[170:173], v234 offset:18432
	ds_read_b128 v[174:177], v234 offset:19456
	ds_read_b128 v[178:181], v234 offset:20480
	ds_read_b128 v[182:185], v234 offset:21504
	ds_read_b128 v[186:189], v234 offset:22528
	ds_read_b128 v[206:209], v234 offset:23552
	global_load_lds_dwordx4 v[210:211], off
	s_add_i32 m0, s69, 0x2000
	s_add_u32 s70, s52, 0x40000
	v_lshl_add_u64 v[212:213], s[52:53], 0, v[200:201]
	s_addc_u32 s71, s53, 0
	s_add_i32 s4, s4, s59
	global_load_lds_dwordx4 v[212:213], off
	v_lshl_add_u64 v[214:215], s[70:71], 0, v[0:1]
	s_mov_b32 m0, s4
	v_lshl_add_u64 v[216:217], s[54:55], 0, v[198:199]
	global_load_lds_dwordx4 v[214:215], off
	v_lshl_add_u64 v[214:215], s[70:71], 0, v[200:201]
	s_add_i32 m0, s4, 0x2000
	s_nop 0
	global_load_lds_dwordx4 v[214:215], off
	v_lshl_add_u64 v[214:215], s[54:55], 0, v[196:197]
	s_mov_b32 m0, s49
	s_nop 0
	global_load_lds_dwordx4 v[214:215], off
	s_mov_b32 m0, s30
	s_nop 0
	global_load_lds_dwordx4 v[216:217], off
	s_waitcnt vmcnt(8)
	s_waitcnt lgkmcnt(0)
	s_barrier
	s_setprio 1
	s_waitcnt lgkmcnt(0)
	v_mfma_f32_16x16x32_bf16 v[62:65], v[130:133], v[162:165], v[62:65]
	v_mfma_f32_16x16x32_bf16 v[58:61], v[138:141], v[162:165], v[58:61]
	v_mfma_f32_16x16x32_bf16 v[50:53], v[130:133], v[170:173], v[50:53]
	v_mfma_f32_16x16x32_bf16 v[42:45], v[138:141], v[170:173], v[42:45]
	v_mfma_f32_16x16x32_bf16 v[34:37], v[130:133], v[178:181], v[34:37]
	v_mfma_f32_16x16x32_bf16 v[26:29], v[138:141], v[178:181], v[26:29]
	v_mfma_f32_16x16x32_bf16 v[18:21], v[130:133], v[186:189], v[18:21]
	v_mfma_f32_16x16x32_bf16 v[10:13], v[138:141], v[186:189], v[10:13]
	v_mfma_f32_16x16x32_bf16 v[62:65], v[134:137], v[166:169], v[62:65]
	v_mfma_f32_16x16x32_bf16 v[58:61], v[142:145], v[166:169], v[58:61]
	v_mfma_f32_16x16x32_bf16 v[50:53], v[134:137], v[174:177], v[50:53]
	v_mfma_f32_16x16x32_bf16 v[42:45], v[142:145], v[174:177], v[42:45]
	v_mfma_f32_16x16x32_bf16 v[34:37], v[134:137], v[182:185], v[34:37]
	v_mfma_f32_16x16x32_bf16 v[26:29], v[142:145], v[182:185], v[26:29]
	v_mfma_f32_16x16x32_bf16 v[18:21], v[134:137], v[206:209], v[18:21]
	v_mfma_f32_16x16x32_bf16 v[10:13], v[142:145], v[206:209], v[10:13]
	s_setprio 0
	s_setprio 1
	v_mfma_f32_16x16x32_bf16 v[54:57], v[146:149], v[162:165], v[54:57]
	v_mfma_f32_16x16x32_bf16 v[46:49], v[154:157], v[162:165], v[46:49]
	v_mfma_f32_16x16x32_bf16 v[38:41], v[146:149], v[170:173], v[38:41]
	v_mfma_f32_16x16x32_bf16 v[30:33], v[154:157], v[170:173], v[30:33]
	v_mfma_f32_16x16x32_bf16 v[22:25], v[146:149], v[178:181], v[22:25]
	v_mfma_f32_16x16x32_bf16 v[14:17], v[154:157], v[178:181], v[14:17]
	v_mfma_f32_16x16x32_bf16 v[6:9], v[146:149], v[186:189], v[6:9]
	v_mfma_f32_16x16x32_bf16 v[2:5], v[154:157], v[186:189], v[2:5]
	v_mfma_f32_16x16x32_bf16 v[54:57], v[150:153], v[166:169], v[54:57]
	v_mfma_f32_16x16x32_bf16 v[46:49], v[158:161], v[166:169], v[46:49]
	v_mfma_f32_16x16x32_bf16 v[38:41], v[150:153], v[174:177], v[38:41]
	v_mfma_f32_16x16x32_bf16 v[30:33], v[158:161], v[174:177], v[30:33]
	v_mfma_f32_16x16x32_bf16 v[22:25], v[150:153], v[182:185], v[22:25]
	v_mfma_f32_16x16x32_bf16 v[14:17], v[158:161], v[182:185], v[14:17]
	v_mfma_f32_16x16x32_bf16 v[6:9], v[150:153], v[206:209], v[6:9]
	v_mfma_f32_16x16x32_bf16 v[2:5], v[158:161], v[206:209], v[2:5]
	s_setprio 0
	s_barrier
	s_add_i32 s4, 0, 0x18000
	s_add_i32 s69, 0, 0x1c000
	v_add_u32_e32 v142, s4, v195
	v_add_u32_e32 v158, s69, v195
	ds_read_b128 v[130:133], v142
	ds_read_b128 v[134:137], v142 offset:1024
	ds_read_b128 v[138:141], v142 offset:2048
	ds_read_b128 v[142:145], v142 offset:3072
	ds_read_b128 v[146:149], v158
	ds_read_b128 v[150:153], v158 offset:1024
	ds_read_b128 v[154:157], v158 offset:2048
	ds_read_b128 v[158:161], v158 offset:3072
	s_add_u32 s54, s54, 0x40000
	s_addc_u32 s55, s55, 0
	s_mov_b32 m0, s31
	v_lshl_add_u64 v[218:219], s[54:55], 0, v[196:197]
	ds_read_b128 v[162:165], v234 offset:32768
	ds_read_b128 v[166:169], v234 offset:33792
	ds_read_b128 v[170:173], v234 offset:34816
	ds_read_b128 v[174:177], v234 offset:35840
	ds_read_b128 v[178:181], v234 offset:36864
	ds_read_b128 v[182:185], v234 offset:37888
	ds_read_b128 v[186:189], v234 offset:38912
	ds_read_b128 v[206:209], v234 offset:39936
	global_load_lds_dwordx4 v[218:219], off
	v_lshl_add_u64 v[218:219], s[54:55], 0, v[198:199]
	s_mov_b32 m0, s60
	s_nop 0
	global_load_lds_dwordx4 v[218:219], off
	s_waitcnt vmcnt(8)
	s_waitcnt lgkmcnt(0)
	s_barrier
	s_setprio 1
	s_waitcnt lgkmcnt(0)
	v_mfma_f32_16x16x32_bf16 v[126:129], v[130:133], v[162:165], v[126:129]
	v_mfma_f32_16x16x32_bf16 v[122:125], v[138:141], v[162:165], v[122:125]
	v_mfma_f32_16x16x32_bf16 v[110:113], v[130:133], v[170:173], v[110:113]
	v_mfma_f32_16x16x32_bf16 v[106:109], v[138:141], v[170:173], v[106:109]
	v_mfma_f32_16x16x32_bf16 v[98:101], v[130:133], v[178:181], v[98:101]
	v_mfma_f32_16x16x32_bf16 v[90:93], v[138:141], v[178:181], v[90:93]
	v_mfma_f32_16x16x32_bf16 v[82:85], v[130:133], v[186:189], v[82:85]
	v_mfma_f32_16x16x32_bf16 v[74:77], v[138:141], v[186:189], v[74:77]
	v_mfma_f32_16x16x32_bf16 v[126:129], v[134:137], v[166:169], v[126:129]
	v_mfma_f32_16x16x32_bf16 v[122:125], v[142:145], v[166:169], v[122:125]
	v_mfma_f32_16x16x32_bf16 v[110:113], v[134:137], v[174:177], v[110:113]
	v_mfma_f32_16x16x32_bf16 v[106:109], v[142:145], v[174:177], v[106:109]
	v_mfma_f32_16x16x32_bf16 v[98:101], v[134:137], v[182:185], v[98:101]
	v_mfma_f32_16x16x32_bf16 v[90:93], v[142:145], v[182:185], v[90:93]
	v_mfma_f32_16x16x32_bf16 v[82:85], v[134:137], v[206:209], v[82:85]
	v_mfma_f32_16x16x32_bf16 v[74:77], v[142:145], v[206:209], v[74:77]
	s_setprio 0
	s_setprio 1
	v_mfma_f32_16x16x32_bf16 v[118:121], v[146:149], v[162:165], v[118:121]
	v_mfma_f32_16x16x32_bf16 v[114:117], v[154:157], v[162:165], v[114:117]
	v_mfma_f32_16x16x32_bf16 v[102:105], v[146:149], v[170:173], v[102:105]
	v_mfma_f32_16x16x32_bf16 v[94:97], v[154:157], v[170:173], v[94:97]
	v_mfma_f32_16x16x32_bf16 v[86:89], v[146:149], v[178:181], v[86:89]
	v_mfma_f32_16x16x32_bf16 v[78:81], v[154:157], v[178:181], v[78:81]
	v_mfma_f32_16x16x32_bf16 v[70:73], v[146:149], v[186:189], v[70:73]
	v_mfma_f32_16x16x32_bf16 v[66:69], v[154:157], v[186:189], v[66:69]
	v_mfma_f32_16x16x32_bf16 v[118:121], v[150:153], v[166:169], v[118:121]
	v_mfma_f32_16x16x32_bf16 v[114:117], v[158:161], v[166:169], v[114:117]
	v_mfma_f32_16x16x32_bf16 v[102:105], v[150:153], v[174:177], v[102:105]
	v_mfma_f32_16x16x32_bf16 v[94:97], v[158:161], v[174:177], v[94:97]
	v_mfma_f32_16x16x32_bf16 v[86:89], v[150:153], v[182:185], v[86:89]
	v_mfma_f32_16x16x32_bf16 v[78:81], v[158:161], v[182:185], v[78:81]
	v_mfma_f32_16x16x32_bf16 v[70:73], v[150:153], v[206:209], v[70:73]
	v_mfma_f32_16x16x32_bf16 v[66:69], v[158:161], v[206:209], v[66:69]
	s_setprio 0
	s_barrier
	s_add_i32 s4, s4, s59
	v_lshl_add_u64 v[210:211], v[210:211], 0, s[22:23]
	s_mov_b32 m0, s4
	ds_read_b128 v[162:165], v234 offset:49152
	ds_read_b128 v[166:169], v234 offset:50176
	ds_read_b128 v[170:173], v234 offset:51200
	ds_read_b128 v[174:177], v234 offset:52224
	ds_read_b128 v[178:181], v234 offset:53248
	ds_read_b128 v[182:185], v234 offset:54272
	ds_read_b128 v[186:189], v234 offset:55296
	ds_read_b128 v[206:209], v234 offset:56320
	global_load_lds_dwordx4 v[210:211], off
	s_add_i32 m0, s4, 0x2000
	s_add_u32 s52, s52, 0x40080
	v_lshl_add_u64 v[210:211], v[212:213], 0, s[22:23]
	s_addc_u32 s53, s53, 0
	s_add_i32 s4, s69, s59
	global_load_lds_dwordx4 v[210:211], off
	v_lshl_add_u64 v[210:211], s[52:53], 0, v[0:1]
	s_mov_b32 m0, s4
	s_nop 0
	global_load_lds_dwordx4 v[210:211], off
	v_lshl_add_u64 v[210:211], s[52:53], 0, v[200:201]
	s_add_i32 m0, s4, 0x2000
	s_nop 0
	global_load_lds_dwordx4 v[210:211], off
	v_lshl_add_u64 v[210:211], v[214:215], 0, s[22:23]
	s_mov_b32 m0, s62
	s_nop 0
	global_load_lds_dwordx4 v[210:211], off
	v_lshl_add_u64 v[210:211], v[216:217], 0, s[22:23]
	s_mov_b32 m0, s63
	s_nop 0
	global_load_lds_dwordx4 v[210:211], off
	s_waitcnt vmcnt(8)
	s_waitcnt lgkmcnt(0)
	s_barrier
	s_setprio 1
	s_waitcnt lgkmcnt(0)
	v_mfma_f32_16x16x32_bf16 v[62:65], v[130:133], v[162:165], v[62:65]
	v_mfma_f32_16x16x32_bf16 v[58:61], v[138:141], v[162:165], v[58:61]
	v_mfma_f32_16x16x32_bf16 v[50:53], v[130:133], v[170:173], v[50:53]
	v_mfma_f32_16x16x32_bf16 v[42:45], v[138:141], v[170:173], v[42:45]
	v_mfma_f32_16x16x32_bf16 v[34:37], v[130:133], v[178:181], v[34:37]
	v_mfma_f32_16x16x32_bf16 v[26:29], v[138:141], v[178:181], v[26:29]
	v_mfma_f32_16x16x32_bf16 v[18:21], v[130:133], v[186:189], v[18:21]
	v_mfma_f32_16x16x32_bf16 v[10:13], v[138:141], v[186:189], v[10:13]
	v_mfma_f32_16x16x32_bf16 v[62:65], v[134:137], v[166:169], v[62:65]
	v_mfma_f32_16x16x32_bf16 v[58:61], v[142:145], v[166:169], v[58:61]
	v_mfma_f32_16x16x32_bf16 v[50:53], v[134:137], v[174:177], v[50:53]
	v_mfma_f32_16x16x32_bf16 v[42:45], v[142:145], v[174:177], v[42:45]
	v_mfma_f32_16x16x32_bf16 v[34:37], v[134:137], v[182:185], v[34:37]
	v_mfma_f32_16x16x32_bf16 v[26:29], v[142:145], v[182:185], v[26:29]
	v_mfma_f32_16x16x32_bf16 v[18:21], v[134:137], v[206:209], v[18:21]
	v_mfma_f32_16x16x32_bf16 v[10:13], v[142:145], v[206:209], v[10:13]
	s_setprio 0
	s_setprio 1
	v_mfma_f32_16x16x32_bf16 v[54:57], v[146:149], v[162:165], v[54:57]
	v_mfma_f32_16x16x32_bf16 v[46:49], v[154:157], v[162:165], v[46:49]
	v_mfma_f32_16x16x32_bf16 v[38:41], v[146:149], v[170:173], v[38:41]
	v_mfma_f32_16x16x32_bf16 v[30:33], v[154:157], v[170:173], v[30:33]
	v_mfma_f32_16x16x32_bf16 v[22:25], v[146:149], v[178:181], v[22:25]
	v_mfma_f32_16x16x32_bf16 v[14:17], v[154:157], v[178:181], v[14:17]
	v_mfma_f32_16x16x32_bf16 v[6:9], v[146:149], v[186:189], v[6:9]
	v_mfma_f32_16x16x32_bf16 v[2:5], v[154:157], v[186:189], v[2:5]
	v_mfma_f32_16x16x32_bf16 v[54:57], v[150:153], v[166:169], v[54:57]
	v_mfma_f32_16x16x32_bf16 v[46:49], v[158:161], v[166:169], v[46:49]
	v_mfma_f32_16x16x32_bf16 v[38:41], v[150:153], v[174:177], v[38:41]
	v_mfma_f32_16x16x32_bf16 v[30:33], v[158:161], v[174:177], v[30:33]
	v_mfma_f32_16x16x32_bf16 v[22:25], v[150:153], v[182:185], v[22:25]
	v_mfma_f32_16x16x32_bf16 v[14:17], v[158:161], v[182:185], v[14:17]
	v_mfma_f32_16x16x32_bf16 v[6:9], v[150:153], v[206:209], v[6:9]
	v_mfma_f32_16x16x32_bf16 v[2:5], v[158:161], v[206:209], v[2:5]
	s_setprio 0
	s_barrier
	s_add_i32 s68, s68, 2
	s_add_u32 s50, s50, 0x100
	s_addc_u32 s51, s51, 0
	s_add_u32 s66, s66, 0x100
	s_addc_u32 s67, s67, 0
	s_cmp_gt_u32 s68, 13
	s_cbranch_scc0 .LBB0_508
	v_lshl_or_b32 v132, s6, 8, v233
	v_lshl_add_u32 v130, s48, 8, v193
	v_ashrrev_i32_e32 v133, 31, v132
	v_lshlrev_b64 v[206:207], 1, v[132:133]
	v_ashrrev_i32_e32 v131, 31, v130
	v_lshl_add_u64 v[132:133], s[40:41], 0, v[206:207]
	v_lshlrev_b64 v[222:223], 11, v[130:131]
	v_lshl_add_u64 v[134:135], v[132:133], 0, v[222:223]
	global_load_dwordx4 v[236:239], v[134:135], off nt
	global_load_dwordx4 v[186:189], v[134:135], off offset:256 nt
	v_or_b32_e32 v134, 16, v130
	v_ashrrev_i32_e32 v135, 31, v134
	v_lshlrev_b64 v[220:221], 11, v[134:135]
	v_lshl_add_u64 v[134:135], v[132:133], 0, v[220:221]
	global_load_dwordx4 v[182:185], v[134:135], off nt
	global_load_dwordx4 v[178:181], v[134:135], off offset:256 nt
	v_or_b32_e32 v134, 32, v130
	v_ashrrev_i32_e32 v135, 31, v134
	v_lshlrev_b64 v[218:219], 11, v[134:135]
	v_lshl_add_u64 v[134:135], v[132:133], 0, v[218:219]
	global_load_dwordx4 v[174:177], v[134:135], off nt
	global_load_dwordx4 v[170:173], v[134:135], off offset:256 nt
	v_or_b32_e32 v130, 48, v130
	v_ashrrev_i32_e32 v131, 31, v130
	v_lshlrev_b64 v[216:217], 11, v[130:131]
	v_lshl_add_u64 v[130:131], v[132:133], 0, v[216:217]
	global_load_dwordx4 v[166:169], v[130:131], off nt
	global_load_dwordx4 v[158:161], v[130:131], off offset:256 nt
	s_mov_b64 s[50:51], 0x40000
	v_lshl_add_u64 v[214:215], v[222:223], 0, s[50:51]
	v_lshl_add_u64 v[130:131], v[132:133], 0, v[214:215]
	global_load_dwordx4 v[162:165], v[130:131], off nt
	global_load_dwordx4 v[154:157], v[130:131], off offset:256 nt
	s_mov_b64 s[50:51], 0x48000
	v_lshl_add_u64 v[212:213], v[222:223], 0, s[50:51]
	v_lshl_add_u64 v[130:131], v[132:133], 0, v[212:213]
	global_load_dwordx4 v[150:153], v[130:131], off nt
	global_load_dwordx4 v[146:149], v[130:131], off offset:256 nt
	s_mov_b64 s[50:51], 0x50000
	v_lshl_add_u64 v[210:211], v[222:223], 0, s[50:51]
	v_lshl_add_u64 v[130:131], v[132:133], 0, v[210:211]
	global_load_dwordx4 v[142:145], v[130:131], off nt
	global_load_dwordx4 v[134:137], v[130:131], off offset:256 nt
	s_mov_b64 s[50:51], 0x58000
	v_lshl_add_u64 v[208:209], v[222:223], 0, s[50:51]
	v_lshl_add_u64 v[130:131], v[132:133], 0, v[208:209]
	global_load_dwordx4 v[138:141], v[130:131], off nt
	s_nop 0
	global_load_dwordx4 v[130:133], v[130:131], off offset:256 nt
	s_and_b64 vcc, exec, s[38:39]
	s_mov_b32 s6, s44
	s_mov_b32 s48, s46
	s_mov_b64 s[52:53], s[36:37]
	s_mov_b64 s[50:51], s[26:27]
	s_waitcnt vmcnt(15)
	v_lshlrev_b32_e32 v230, 16, v236
	v_and_b32_e32 v231, 0xffff0000, v236
	v_lshlrev_b32_e32 v236, 16, v237
	v_and_b32_e32 v237, 0xffff0000, v237
	v_pk_add_f32 v[128:129], v[128:129], v[236:237]
	v_pk_add_f32 v[126:127], v[126:127], v[230:231]
	v_lshlrev_b32_e32 v230, 16, v238
	v_and_b32_e32 v231, 0xffff0000, v238
	v_lshlrev_b32_e32 v236, 16, v239
	v_and_b32_e32 v237, 0xffff0000, v239
	v_pk_add_f32 v[236:237], v[124:125], v[236:237]
	v_pk_add_f32 v[124:125], v[122:123], v[230:231]
	v_cvt_pk_bf16_f32 v122, v126, v127
	v_lshl_add_u64 v[126:127], s[42:43], 0, v[222:223]
	v_cvt_pk_bf16_f32 v123, v128, v129
	v_cvt_pk_bf16_f32 v124, v124, v125
	v_cvt_pk_bf16_f32 v125, v236, v237
	v_lshl_add_u64 v[126:127], v[126:127], 0, v[206:207]
	global_store_dwordx4 v[126:127], v[122:125], off
	s_nop 1
	s_waitcnt vmcnt(15)
	v_lshlrev_b32_e32 v122, 16, v186
	v_and_b32_e32 v123, 0xffff0000, v186
	v_lshlrev_b32_e32 v124, 16, v187
	v_and_b32_e32 v125, 0xffff0000, v187
	v_pk_add_f32 v[120:121], v[120:121], v[124:125]
	v_pk_add_f32 v[118:119], v[118:119], v[122:123]
	v_lshlrev_b32_e32 v122, 16, v188
	v_and_b32_e32 v123, 0xffff0000, v188
	v_lshlrev_b32_e32 v124, 16, v189
	v_and_b32_e32 v125, 0xffff0000, v189
	v_pk_add_f32 v[124:125], v[116:117], v[124:125]
	v_pk_add_f32 v[116:117], v[114:115], v[122:123]
	v_cvt_pk_bf16_f32 v114, v118, v119
	v_cvt_pk_bf16_f32 v115, v120, v121
	v_cvt_pk_bf16_f32 v116, v116, v117
	v_cvt_pk_bf16_f32 v117, v124, v125
	global_store_dwordx4 v[126:127], v[114:117], off offset:256
	s_nop 1
	s_waitcnt vmcnt(15)
	v_lshlrev_b32_e32 v114, 16, v182
	v_and_b32_e32 v115, 0xffff0000, v182
	v_lshlrev_b32_e32 v116, 16, v183
	v_and_b32_e32 v117, 0xffff0000, v183
	v_pk_add_f32 v[112:113], v[112:113], v[116:117]
	v_pk_add_f32 v[110:111], v[110:111], v[114:115]
	v_lshlrev_b32_e32 v114, 16, v184
	v_and_b32_e32 v115, 0xffff0000, v184
	v_lshlrev_b32_e32 v116, 16, v185
	v_and_b32_e32 v117, 0xffff0000, v185
	v_pk_add_f32 v[116:117], v[108:109], v[116:117]
	v_pk_add_f32 v[108:109], v[106:107], v[114:115]
	v_cvt_pk_bf16_f32 v106, v110, v111
	v_lshl_add_u64 v[110:111], s[42:43], 0, v[220:221]
	v_cvt_pk_bf16_f32 v107, v112, v113
	v_cvt_pk_bf16_f32 v108, v108, v109
	v_cvt_pk_bf16_f32 v109, v116, v117
	v_lshl_add_u64 v[110:111], v[110:111], 0, v[206:207]
	global_store_dwordx4 v[110:111], v[106:109], off
	s_nop 1
	s_waitcnt vmcnt(15)
	v_lshlrev_b32_e32 v106, 16, v178
	v_and_b32_e32 v107, 0xffff0000, v178
	v_lshlrev_b32_e32 v108, 16, v179
	v_and_b32_e32 v109, 0xffff0000, v179
	v_pk_add_f32 v[104:105], v[104:105], v[108:109]
	v_pk_add_f32 v[102:103], v[102:103], v[106:107]
	v_lshlrev_b32_e32 v106, 16, v180
	v_and_b32_e32 v107, 0xffff0000, v180
	v_lshlrev_b32_e32 v108, 16, v181
	v_and_b32_e32 v109, 0xffff0000, v181
	v_pk_add_f32 v[108:109], v[96:97], v[108:109]
	v_pk_add_f32 v[96:97], v[94:95], v[106:107]
	v_cvt_pk_bf16_f32 v94, v102, v103
	v_cvt_pk_bf16_f32 v95, v104, v105
	v_cvt_pk_bf16_f32 v96, v96, v97
	v_cvt_pk_bf16_f32 v97, v108, v109
	global_store_dwordx4 v[110:111], v[94:97], off offset:256
	s_nop 1
	s_waitcnt vmcnt(15)
	v_lshlrev_b32_e32 v94, 16, v174
	v_and_b32_e32 v95, 0xffff0000, v174
	v_lshlrev_b32_e32 v96, 16, v175
	v_and_b32_e32 v97, 0xffff0000, v175
	v_pk_add_f32 v[96:97], v[100:101], v[96:97]
	v_pk_add_f32 v[94:95], v[98:99], v[94:95]
	v_lshlrev_b32_e32 v98, 16, v176
	v_and_b32_e32 v99, 0xffff0000, v176
	v_lshlrev_b32_e32 v100, 16, v177
	v_and_b32_e32 v101, 0xffff0000, v177
	v_pk_add_f32 v[100:101], v[92:93], v[100:101]
	v_pk_add_f32 v[92:93], v[90:91], v[98:99]
	v_cvt_pk_bf16_f32 v90, v94, v95
	v_lshl_add_u64 v[94:95], s[42:43], 0, v[218:219]
	v_cvt_pk_bf16_f32 v91, v96, v97
	v_cvt_pk_bf16_f32 v92, v92, v93
	v_cvt_pk_bf16_f32 v93, v100, v101
	v_lshl_add_u64 v[94:95], v[94:95], 0, v[206:207]
	global_store_dwordx4 v[94:95], v[90:93], off
	s_nop 1
	s_waitcnt vmcnt(15)
	v_lshlrev_b32_e32 v90, 16, v170
	v_and_b32_e32 v91, 0xffff0000, v170
	v_lshlrev_b32_e32 v92, 16, v171
	v_and_b32_e32 v93, 0xffff0000, v171
	v_pk_add_f32 v[88:89], v[88:89], v[92:93]
	v_pk_add_f32 v[86:87], v[86:87], v[90:91]
	v_lshlrev_b32_e32 v90, 16, v172
	v_and_b32_e32 v91, 0xffff0000, v172
	v_lshlrev_b32_e32 v92, 16, v173
	v_and_b32_e32 v93, 0xffff0000, v173
	v_pk_add_f32 v[92:93], v[80:81], v[92:93]
	v_pk_add_f32 v[80:81], v[78:79], v[90:91]
	v_cvt_pk_bf16_f32 v78, v86, v87
	v_cvt_pk_bf16_f32 v79, v88, v89
	v_cvt_pk_bf16_f32 v80, v80, v81
	v_cvt_pk_bf16_f32 v81, v92, v93
	global_store_dwordx4 v[94:95], v[78:81], off offset:256
	s_nop 1
	s_waitcnt vmcnt(15)
	v_lshlrev_b32_e32 v78, 16, v166
	v_and_b32_e32 v79, 0xffff0000, v166
	v_lshlrev_b32_e32 v80, 16, v167
	v_and_b32_e32 v81, 0xffff0000, v167
	v_pk_add_f32 v[80:81], v[84:85], v[80:81]
	v_pk_add_f32 v[78:79], v[82:83], v[78:79]
	v_lshlrev_b32_e32 v82, 16, v168
	v_and_b32_e32 v83, 0xffff0000, v168
	v_lshlrev_b32_e32 v84, 16, v169
	v_and_b32_e32 v85, 0xffff0000, v169
	v_pk_add_f32 v[84:85], v[76:77], v[84:85]
	v_pk_add_f32 v[76:77], v[74:75], v[82:83]
	v_cvt_pk_bf16_f32 v74, v78, v79
	v_lshl_add_u64 v[78:79], s[42:43], 0, v[216:217]
	v_cvt_pk_bf16_f32 v75, v80, v81
	v_cvt_pk_bf16_f32 v76, v76, v77
	v_cvt_pk_bf16_f32 v77, v84, v85
	v_lshl_add_u64 v[78:79], v[78:79], 0, v[206:207]
	global_store_dwordx4 v[78:79], v[74:77], off
	s_nop 1
	s_waitcnt vmcnt(15)
	v_lshlrev_b32_e32 v74, 16, v158
	v_and_b32_e32 v75, 0xffff0000, v158
	v_lshlrev_b32_e32 v76, 16, v159
	v_and_b32_e32 v77, 0xffff0000, v159
	v_pk_add_f32 v[72:73], v[72:73], v[76:77]
	v_pk_add_f32 v[70:71], v[70:71], v[74:75]
	v_lshlrev_b32_e32 v74, 16, v160
	v_and_b32_e32 v75, 0xffff0000, v160
	v_lshlrev_b32_e32 v76, 16, v161
	v_and_b32_e32 v77, 0xffff0000, v161
	v_pk_add_f32 v[76:77], v[68:69], v[76:77]
	v_pk_add_f32 v[68:69], v[66:67], v[74:75]
	v_cvt_pk_bf16_f32 v66, v70, v71
	v_cvt_pk_bf16_f32 v67, v72, v73
	v_cvt_pk_bf16_f32 v68, v68, v69
	v_cvt_pk_bf16_f32 v69, v76, v77
	global_store_dwordx4 v[78:79], v[66:69], off offset:256
	s_nop 1
	s_waitcnt vmcnt(15)
	v_lshlrev_b32_e32 v66, 16, v162
	v_and_b32_e32 v67, 0xffff0000, v162
	v_lshlrev_b32_e32 v68, 16, v163
	v_and_b32_e32 v69, 0xffff0000, v163
	v_pk_add_f32 v[64:65], v[64:65], v[68:69]
	v_pk_add_f32 v[62:63], v[62:63], v[66:67]
	v_lshlrev_b32_e32 v66, 16, v164
	v_and_b32_e32 v67, 0xffff0000, v164
	v_lshlrev_b32_e32 v68, 16, v165
	v_and_b32_e32 v69, 0xffff0000, v165
	v_pk_add_f32 v[68:69], v[60:61], v[68:69]
	v_pk_add_f32 v[60:61], v[58:59], v[66:67]
	v_cvt_pk_bf16_f32 v58, v62, v63
	v_lshl_add_u64 v[62:63], s[42:43], 0, v[214:215]
	v_cvt_pk_bf16_f32 v59, v64, v65
	v_cvt_pk_bf16_f32 v60, v60, v61
	v_cvt_pk_bf16_f32 v61, v68, v69
	v_lshl_add_u64 v[62:63], v[62:63], 0, v[206:207]
	global_store_dwordx4 v[62:63], v[58:61], off
	s_nop 1
	s_waitcnt vmcnt(15)
	v_lshlrev_b32_e32 v58, 16, v154
	v_and_b32_e32 v59, 0xffff0000, v154
	v_lshlrev_b32_e32 v60, 16, v155
	v_and_b32_e32 v61, 0xffff0000, v155
	v_pk_add_f32 v[56:57], v[56:57], v[60:61]
	v_pk_add_f32 v[54:55], v[54:55], v[58:59]
	v_lshlrev_b32_e32 v58, 16, v156
	v_and_b32_e32 v59, 0xffff0000, v156
	v_lshlrev_b32_e32 v60, 16, v157
	v_and_b32_e32 v61, 0xffff0000, v157
	v_pk_add_f32 v[60:61], v[48:49], v[60:61]
	v_pk_add_f32 v[48:49], v[46:47], v[58:59]
	v_cvt_pk_bf16_f32 v46, v54, v55
	v_cvt_pk_bf16_f32 v47, v56, v57
	v_cvt_pk_bf16_f32 v48, v48, v49
	v_cvt_pk_bf16_f32 v49, v60, v61
	global_store_dwordx4 v[62:63], v[46:49], off offset:256
	s_nop 1
	s_waitcnt vmcnt(15)
	v_lshlrev_b32_e32 v46, 16, v150
	v_and_b32_e32 v47, 0xffff0000, v150
	v_lshlrev_b32_e32 v48, 16, v151
	v_and_b32_e32 v49, 0xffff0000, v151
	v_pk_add_f32 v[48:49], v[52:53], v[48:49]
	v_pk_add_f32 v[46:47], v[50:51], v[46:47]
	v_lshlrev_b32_e32 v50, 16, v152
	v_and_b32_e32 v51, 0xffff0000, v152
	v_lshlrev_b32_e32 v52, 16, v153
	v_and_b32_e32 v53, 0xffff0000, v153
	v_pk_add_f32 v[52:53], v[44:45], v[52:53]
	v_pk_add_f32 v[44:45], v[42:43], v[50:51]
	v_cvt_pk_bf16_f32 v42, v46, v47
	v_lshl_add_u64 v[46:47], s[42:43], 0, v[212:213]
	v_cvt_pk_bf16_f32 v43, v48, v49
	v_cvt_pk_bf16_f32 v44, v44, v45
	v_cvt_pk_bf16_f32 v45, v52, v53
	v_lshl_add_u64 v[46:47], v[46:47], 0, v[206:207]
	global_store_dwordx4 v[46:47], v[42:45], off
	s_nop 1
	s_waitcnt vmcnt(15)
	v_lshlrev_b32_e32 v42, 16, v146
	v_and_b32_e32 v43, 0xffff0000, v146
	v_lshlrev_b32_e32 v44, 16, v147
	v_and_b32_e32 v45, 0xffff0000, v147
	v_pk_add_f32 v[40:41], v[40:41], v[44:45]
	v_pk_add_f32 v[38:39], v[38:39], v[42:43]
	v_lshlrev_b32_e32 v42, 16, v148
	v_and_b32_e32 v43, 0xffff0000, v148
	v_lshlrev_b32_e32 v44, 16, v149
	v_and_b32_e32 v45, 0xffff0000, v149
	v_pk_add_f32 v[44:45], v[32:33], v[44:45]
	v_pk_add_f32 v[32:33], v[30:31], v[42:43]
	v_cvt_pk_bf16_f32 v30, v38, v39
	v_cvt_pk_bf16_f32 v31, v40, v41
	v_cvt_pk_bf16_f32 v32, v32, v33
	v_cvt_pk_bf16_f32 v33, v44, v45
	global_store_dwordx4 v[46:47], v[30:33], off offset:256
	s_nop 1
	s_waitcnt vmcnt(15)
	v_lshlrev_b32_e32 v30, 16, v142
	v_and_b32_e32 v31, 0xffff0000, v142
	v_lshlrev_b32_e32 v32, 16, v143
	v_and_b32_e32 v33, 0xffff0000, v143
	v_pk_add_f32 v[32:33], v[36:37], v[32:33]
	v_pk_add_f32 v[30:31], v[34:35], v[30:31]
	v_lshlrev_b32_e32 v34, 16, v144
	v_and_b32_e32 v35, 0xffff0000, v144
	v_lshlrev_b32_e32 v36, 16, v145
	v_and_b32_e32 v37, 0xffff0000, v145
	v_pk_add_f32 v[36:37], v[28:29], v[36:37]
	v_pk_add_f32 v[28:29], v[26:27], v[34:35]
	v_cvt_pk_bf16_f32 v26, v30, v31
	v_lshl_add_u64 v[30:31], s[42:43], 0, v[210:211]
	v_cvt_pk_bf16_f32 v27, v32, v33
	v_cvt_pk_bf16_f32 v28, v28, v29
	v_cvt_pk_bf16_f32 v29, v36, v37
	v_lshl_add_u64 v[30:31], v[30:31], 0, v[206:207]
	global_store_dwordx4 v[30:31], v[26:29], off
	s_nop 1
	s_waitcnt vmcnt(15)
	v_lshlrev_b32_e32 v26, 16, v134
	v_and_b32_e32 v27, 0xffff0000, v134
	v_lshlrev_b32_e32 v28, 16, v135
	v_and_b32_e32 v29, 0xffff0000, v135
	v_pk_add_f32 v[24:25], v[24:25], v[28:29]
	v_pk_add_f32 v[22:23], v[22:23], v[26:27]
	v_lshlrev_b32_e32 v26, 16, v136
	v_and_b32_e32 v27, 0xffff0000, v136
	v_lshlrev_b32_e32 v28, 16, v137
	v_and_b32_e32 v29, 0xffff0000, v137
	v_pk_add_f32 v[28:29], v[16:17], v[28:29]
	v_pk_add_f32 v[16:17], v[14:15], v[26:27]
	v_cvt_pk_bf16_f32 v14, v22, v23
	v_cvt_pk_bf16_f32 v15, v24, v25
	v_cvt_pk_bf16_f32 v16, v16, v17
	v_cvt_pk_bf16_f32 v17, v28, v29
	global_store_dwordx4 v[30:31], v[14:17], off offset:256
	s_nop 1
	s_waitcnt vmcnt(15)
	v_lshlrev_b32_e32 v14, 16, v138
	v_and_b32_e32 v15, 0xffff0000, v138
	v_lshlrev_b32_e32 v16, 16, v139
	v_and_b32_e32 v17, 0xffff0000, v139
	v_pk_add_f32 v[16:17], v[20:21], v[16:17]
	v_pk_add_f32 v[14:15], v[18:19], v[14:15]
	v_lshlrev_b32_e32 v18, 16, v140
	v_and_b32_e32 v19, 0xffff0000, v140
	v_lshlrev_b32_e32 v20, 16, v141
	v_and_b32_e32 v21, 0xffff0000, v141
	v_pk_add_f32 v[20:21], v[12:13], v[20:21]
	v_pk_add_f32 v[12:13], v[10:11], v[18:19]
	v_cvt_pk_bf16_f32 v10, v14, v15
	v_lshl_add_u64 v[14:15], s[42:43], 0, v[208:209]
	v_cvt_pk_bf16_f32 v11, v16, v17
	v_cvt_pk_bf16_f32 v12, v12, v13
	v_cvt_pk_bf16_f32 v13, v20, v21
	v_lshl_add_u64 v[14:15], v[14:15], 0, v[206:207]
	global_store_dwordx4 v[14:15], v[10:13], off
	s_nop 1
	s_waitcnt vmcnt(15)
	v_lshlrev_b32_e32 v10, 16, v130
	v_and_b32_e32 v11, 0xffff0000, v130
	v_lshlrev_b32_e32 v12, 16, v131
	v_and_b32_e32 v13, 0xffff0000, v131
	v_pk_add_f32 v[8:9], v[8:9], v[12:13]
	v_pk_add_f32 v[6:7], v[6:7], v[10:11]
	v_lshlrev_b32_e32 v10, 16, v132
	v_and_b32_e32 v11, 0xffff0000, v132
	v_lshlrev_b32_e32 v12, 16, v133
	v_and_b32_e32 v13, 0xffff0000, v133
	v_pk_add_f32 v[12:13], v[4:5], v[12:13]
	v_pk_add_f32 v[4:5], v[2:3], v[10:11]
	v_cvt_pk_bf16_f32 v2, v6, v7
	v_cvt_pk_bf16_f32 v3, v8, v9
	v_cvt_pk_bf16_f32 v4, v4, v5
	v_cvt_pk_bf16_f32 v5, v12, v13
	global_store_dwordx4 v[14:15], v[2:5], off offset:256
	s_cbranch_vccz .LBB0_501
	s_waitcnt vmcnt(0)
	s_cmpk_gt_u32 s14, 0xff
	s_cbranch_scc1 .LBB0_512
	s_barrier
